# attention loop: DMA addresses of tile t+2 formed before the barrier and the five LDS-DMA issues moved into the QK MFMA shadow (strategy 8), with QK/PV read-ahead
# baseline (speedup 1.0000x reference)
; #define LAS __attribute__((address_space(3)))
; #define SBAR() __builtin_amdgcn_sched_barrier(0)
; __device__ __forceinline__ void qkt(f32x16& p0, f32x16& p1, LAS unsigned char* lds  , int r32, int hi, const bf16x8* qr) {
;     p0 = f32x16{}; p1 = f32x16{};
;     const LAS unsigned char* kb[4];
; #pragma unroll
;     for (int dd = 0; dd < 4; ++dd) kb[dd] = lds + K_OFF + KSWZ(r32, (dd * 16 + hi * 8) * 2);
; #pragma unroll
;     for (int d0 = 0; d0 < 8; ++d0) { const LAS unsigned char* a = kb[d0 & 3] + (d0 >> 2) * 128;
;         const bf16x8 b0 = *(const LAS bf16x8*)(a);
;         const bf16x8 b1 = *(const LAS bf16x8*)(a + 32 * 256);
;         p0 = __builtin_amdgcn_mfma_f32_32x32x16_bf16(b0, qr[d0], p0, 0, 0, 0);
;         p1 = __builtin_amdgcn_mfma_f32_32x32x16_bf16(b1, qr[d0], p1, 0, 0, 0); }
; #pragma unroll
;     for (int e = 0; e < 4; ++e) { const LAS unsigned char* a = lds + P_OFF + KPSWZ(r32, (e * 2 + hi) * 16);
;         const bf16x8 b0 = *(const LAS bf16x8*)(a);
;         const bf16x8 b1 = *(const LAS bf16x8*)(a + 32 * 128);
;         p0 = __builtin_amdgcn_mfma_f32_32x32x16_bf16(b0, qr[8 + e], p0, 0, 0, 0);
;         p1 = __builtin_amdgcn_mfma_f32_32x32x16_bf16(b1, qr[8 + e], p1, 0, 0, 0); }
; }
; __device__ __forceinline__ void attn_unit(LAS unsigned char* lds, int b, int h, int qb, const bf16* Q  , const bf16* KV  , const bf16* KPE  ,
;                                           const float* ROPE  , bf16* O  , const int wave_) {
;     ...
;     float m_reg = -1e30f, l_reg = 0.f; f32x16 o[4] = {};
;     f32x16 p0, p1; float mn, alpha; bf16x8 pa0, pa1, pa2, pa3;
;     asm volatile("s_waitcnt vmcnt(0)" ::: "memory");
;     AISSUE(0, 0); AISSUE(1, BUFB);
;     int bc = 0, bl = 2 * BUFB;
;     for (int t = 0; t < NT; ++t) {
;         asm volatile("s_waitcnt vmcnt(5)" ::: "memory"); __builtin_amdgcn_s_barrier();
;         { const int tn = (t + 2 < NT) ? t + 2 : NT - 1; AISSUE(tn, bl); }
;         const int kb_ = t * KVBLK;
;         if (kb_ <= qlo + 31) {
;             SBAR(); qkt(p0, p1, lds + bc, r32, hi, qr);
.LBB0_720:
	s_add_i32 s4, s73, 2
	s_min_u32 s70, s4, s2
	s_lshl_b64 s[4:5], s[70:71], 18
	s_add_u32 s4, s96, s4
	s_addc_u32 s5, s97, s5
	s_lshl_b64 s[6:7], s[70:71], 13
	v_lshl_add_u64 v[240:241], v[150:151], 1, s[4:5]
	v_lshl_add_u64 v[242:243], v[152:153], 1, s[4:5]
	v_lshl_add_u64 v[244:245], v[146:147], 1, s[4:5]
	v_lshl_add_u64 v[246:247], v[148:149], 1, s[4:5]
	v_lshl_add_u64 v[248:249], v[154:155], 0, s[6:7]
	v_lshl_add_u64 v[240:241], v[240:241], 0, s[66:67]
	v_lshl_add_u64 v[242:243], v[242:243], 0, s[66:67]
	s_add_i32 s8, s95, s69
	s_sub_i32 s4, s94, 63
	s_waitcnt vmcnt(5)
	s_barrier
	s_cmp_gt_i32 s4, s68
	s_cbranch_scc1 .Lattn_inactive
	s_add_i32 s4, s72, 0
	v_add_u32_e32 v216, s4, v160
	v_add_u32_e32 v220, s4, v166
	v_add_u32_e32 v217, v216, v162
	v_add_u32_e32 v218, v216, v163
	v_add_u32_e32 v219, v216, v165
	v_add_u32_e32 v216, v216, v161
	v_add_u32_e32 v221, v220, v168
	v_add_u32_e32 v222, v220, v169
	v_add_u32_e32 v223, v220, v170
	v_add_u32_e32 v220, v220, v167
	ds_read_b128 v[176:179], v216 offset:16384
	ds_read_b128 v[180:183], v216 offset:24576
	ds_read_b128 v[184:187], v217 offset:16384
	ds_read_b128 v[188:191], v217 offset:24576
	ds_read_b128 v[192:195], v218 offset:16384
	ds_read_b128 v[196:199], v218 offset:24576
	ds_read_b128 v[200:203], v219 offset:16384
	ds_read_b128 v[204:207], v219 offset:24576
	ds_read_b128 v[208:211], v216 offset:16512
	ds_read_b128 v[212:215], v216 offset:24704
	s_waitcnt lgkmcnt(8)
	v_mfma_f32_32x32x16_bf16 v[80:95], v[176:179], v[124:127], 0
	v_mfma_f32_32x32x16_bf16 v[64:79], v[180:183], v[124:127], 0
	ds_read_b128 v[176:179], v217 offset:16512
	ds_read_b128 v[180:183], v217 offset:24704
	s_mov_b32 m0, s8
	s_waitcnt lgkmcnt(8)
	v_mfma_f32_32x32x16_bf16 v[80:95], v[184:187], v[100:103], v[80:95]
	v_mfma_f32_32x32x16_bf16 v[64:79], v[188:191], v[100:103], v[64:79]
	global_load_lds_dwordx4 v[240:241], off
	ds_read_b128 v[184:187], v218 offset:16512
	ds_read_b128 v[188:191], v218 offset:24704
	s_waitcnt lgkmcnt(8)
	v_mfma_f32_32x32x16_bf16 v[80:95], v[192:195], v[104:107], v[80:95]
	v_mfma_f32_32x32x16_bf16 v[64:79], v[196:199], v[104:107], v[64:79]
	ds_read_b128 v[192:195], v219 offset:16512
	ds_read_b128 v[196:199], v219 offset:24704
	s_add_i32 m0, s8, 0x2000
	s_waitcnt lgkmcnt(8)
	v_mfma_f32_32x32x16_bf16 v[80:95], v[200:203], v[108:111], v[80:95]
	v_mfma_f32_32x32x16_bf16 v[64:79], v[204:207], v[108:111], v[64:79]
	global_load_lds_dwordx4 v[242:243], off
	ds_read_b128 v[200:203], v220 offset:32768
	ds_read_b128 v[204:207], v220 offset:36864
	s_waitcnt lgkmcnt(8)
	v_mfma_f32_32x32x16_bf16 v[80:95], v[208:211], v[112:115], v[80:95]
	v_mfma_f32_32x32x16_bf16 v[64:79], v[212:215], v[112:115], v[64:79]
	ds_read_b128 v[208:211], v221 offset:32768
	ds_read_b128 v[212:215], v221 offset:36864
	s_add_i32 m0, s8, 0x4000
	s_waitcnt lgkmcnt(8)
	v_mfma_f32_32x32x16_bf16 v[80:95], v[176:179], v[116:119], v[80:95]
	v_mfma_f32_32x32x16_bf16 v[64:79], v[180:183], v[116:119], v[64:79]
	global_load_lds_dwordx4 v[244:245], off
	ds_read_b128 v[176:179], v222 offset:32768
	ds_read_b128 v[180:183], v222 offset:36864
	s_waitcnt lgkmcnt(8)
	v_mfma_f32_32x32x16_bf16 v[80:95], v[184:187], v[120:123], v[80:95]
	v_mfma_f32_32x32x16_bf16 v[64:79], v[188:191], v[120:123], v[64:79]
	ds_read_b128 v[184:187], v223 offset:32768
	ds_read_b128 v[188:191], v223 offset:36864
	s_add_i32 m0, s8, 0x6000
	s_waitcnt lgkmcnt(8)
	v_mfma_f32_32x32x16_bf16 v[80:95], v[192:195], v[96:99], v[80:95]
	v_mfma_f32_32x32x16_bf16 v[64:79], v[196:199], v[96:99], v[64:79]
	global_load_lds_dwordx4 v[246:247], off
	s_waitcnt lgkmcnt(6)
	v_mfma_f32_32x32x16_bf16 v[80:95], v[200:203], v[128:131], v[80:95]
	v_mfma_f32_32x32x16_bf16 v[64:79], v[204:207], v[128:131], v[64:79]
	s_add_i32 m0, s8, 0x8000
	s_waitcnt lgkmcnt(4)
	v_mfma_f32_32x32x16_bf16 v[80:95], v[208:211], v[136:139], v[80:95]
	v_mfma_f32_32x32x16_bf16 v[64:79], v[212:215], v[136:139], v[64:79]
	global_load_lds_dwordx4 v[248:249], off
	s_waitcnt lgkmcnt(2)
	v_mfma_f32_32x32x16_bf16 v[80:95], v[176:179], v[132:135], v[80:95]
	v_mfma_f32_32x32x16_bf16 v[64:79], v[180:183], v[132:135], v[64:79]
	s_waitcnt lgkmcnt(0)
	v_mfma_f32_32x32x16_bf16 v[80:95], v[184:187], v[140:143], v[80:95]
	v_mfma_f32_32x32x16_bf16 v[64:79], v[188:191], v[140:143], v[64:79]
	s_cmp_le_i32 s94, s33
	v_add_u32_e32 v252, s72, v171
	ds_read_b64_tr_b16 v[224:225], v252 offset:0
	ds_read_b64_tr_b16 v[226:227], v252 offset:2048
	ds_read_b64_tr_b16 v[228:229], v252 offset:4096
	ds_read_b64_tr_b16 v[230:231], v252 offset:6144
	ds_read_b64_tr_b16 v[232:233], v252 offset:8192
	ds_read_b64_tr_b16 v[234:235], v252 offset:10240
	ds_read_b64_tr_b16 v[236:237], v252 offset:12288
	ds_read_b64_tr_b16 v[238:239], v252 offset:14336
	s_cbranch_scc1 .LBB0_723
; __device__ __forceinline__ void mask_tile(f32x16& p0, f32x16& p1, int dq) {
;     const float NEG = -__builtin_inff();
; #pragma unroll
;     for (int r = 0; r < 16; ++r) { const int c = (r & 3) + 8 * (r >> 2);
;         if (dq - c < 0) p0[r] = NEG;
;         if (dq - c - 32 < 0) p1[r] = NEG; }
; }
	v_cmp_gt_i32_e64 s[62:63], 26, v172
	v_cmp_gt_i32_e64 s[64:65], 27, v172
	v_cmp_gt_i32_e64 s[60:61], 25, v172
	s_and_b64 s[62:63], s[64:65], s[62:63]
	v_cmp_gt_i32_e64 s[58:59], 24, v172
	s_and_b64 s[60:61], s[62:63], s[60:61]
	v_cmp_gt_i32_e64 s[56:57], 19, v172
	s_and_b64 s[58:59], s[60:61], s[58:59]
	v_cmp_gt_i32_e64 s[54:55], 18, v172
	s_and_b64 s[56:57], s[58:59], s[56:57]
	v_cmp_gt_i32_e64 s[52:53], 17, v172
	s_and_b64 s[54:55], s[56:57], s[54:55]
	v_cmp_gt_i32_e64 s[50:51], 16, v172
	s_and_b64 s[52:53], s[54:55], s[52:53]
	v_cmp_gt_i32_e64 s[48:49], 11, v172
	s_and_b64 s[50:51], s[52:53], s[50:51]
	v_cmp_gt_i32_e64 s[46:47], 10, v172
	s_and_b64 s[48:49], s[50:51], s[48:49]
	v_cmp_gt_i32_e64 s[44:45], 9, v172
	s_and_b64 s[46:47], s[48:49], s[46:47]
	v_cmp_gt_i32_e64 s[42:43], 8, v172
	s_and_b64 s[44:45], s[46:47], s[44:45]
	v_cmp_gt_i32_e64 s[40:41], 3, v172
	s_and_b64 s[42:43], s[44:45], s[42:43]
	v_cmp_gt_i32_e64 s[38:39], 2, v172
	s_and_b64 s[40:41], s[42:43], s[40:41]
	v_cmp_gt_i32_e64 s[36:37], 1, v172
	s_and_b64 s[38:39], s[40:41], s[38:39]
	v_cmp_gt_i32_e64 s[34:35], 0, v172
	s_and_b64 s[36:37], s[38:39], s[36:37]
	s_and_b64 s[34:35], s[36:37], s[34:35]
	v_cmp_gt_i32_e64 s[30:31], 58, v172
	v_cndmask_b32_e64 v80, v80, v173, s[34:35]
	v_cmp_gt_i32_e64 s[34:35], 59, v172
	v_cmp_gt_i32_e64 s[28:29], 57, v172
	s_and_b64 s[30:31], s[34:35], s[30:31]
	v_cmp_gt_i32_e64 s[26:27], 56, v172
	s_and_b64 s[28:29], s[30:31], s[28:29]
	v_cmp_gt_i32_e64 s[24:25], 51, v172
	s_and_b64 s[26:27], s[28:29], s[26:27]
	v_cmp_gt_i32_e64 s[22:23], 50, v172
	s_and_b64 s[24:25], s[26:27], s[24:25]
	v_cmp_gt_i32_e64 s[20:21], 49, v172
	s_and_b64 s[22:23], s[24:25], s[22:23]
	v_cmp_gt_i32_e64 s[18:19], 48, v172
	s_and_b64 s[20:21], s[22:23], s[20:21]
	v_cmp_gt_i32_e64 s[16:17], 43, v172
	s_and_b64 s[18:19], s[20:21], s[18:19]
	v_cmp_gt_i32_e64 s[14:15], 42, v172
	s_and_b64 s[16:17], s[18:19], s[16:17]
	v_cmp_gt_i32_e64 s[12:13], 41, v172
	s_and_b64 s[14:15], s[16:17], s[14:15]
	v_cmp_gt_i32_e64 s[10:11], 40, v172
	s_and_b64 s[12:13], s[14:15], s[12:13]
	v_cmp_gt_i32_e64 s[8:9], 35, v172
	s_and_b64 s[10:11], s[12:13], s[10:11]
	v_cmp_gt_i32_e64 s[6:7], 34, v172
	s_and_b64 s[8:9], s[10:11], s[8:9]
	v_cmp_gt_i32_e64 s[4:5], 33, v172
	v_cndmask_b32_e64 v94, v94, v173, s[62:63]
	v_cndmask_b32_e64 v93, v93, v173, s[60:61]
	v_cndmask_b32_e64 v92, v92, v173, s[58:59]
	v_cndmask_b32_e64 v91, v91, v173, s[56:57]
	v_cndmask_b32_e64 v90, v90, v173, s[54:55]
	v_cndmask_b32_e64 v89, v89, v173, s[52:53]
	v_cndmask_b32_e64 v88, v88, v173, s[50:51]
	v_cndmask_b32_e64 v87, v87, v173, s[48:49]
	v_readlane_b32 s48, v254, 42
	s_and_b64 s[6:7], s[8:9], s[6:7]
	v_cmp_gt_i32_e32 vcc, 32, v172
	v_readlane_b32 s52, v254, 46
	v_readlane_b32 s53, v254, 47
	v_readlane_b32 s56, v254, 50
	v_readlane_b32 s57, v254, 51
	v_readlane_b32 s58, v254, 52
	v_readlane_b32 s59, v254, 53
	v_readlane_b32 s60, v254, 54
	v_readlane_b32 s61, v254, 55
	s_and_b64 s[4:5], s[6:7], s[4:5]
	v_readlane_b32 s62, v254, 56
	v_readlane_b32 s63, v254, 57
	s_mov_b64 s[52:53], s[56:57]
	s_mov_b64 s[56:57], s[60:61]
	s_and_b64 vcc, s[4:5], vcc
	v_cndmask_b32_e64 v95, v95, v173, s[64:65]
	s_mov_b64 s[58:59], s[62:63]
	v_cndmask_b32_e64 v86, v86, v173, s[46:47]
	v_cndmask_b32_e64 v85, v85, v173, s[44:45]
	v_cndmask_b32_e64 v84, v84, v173, s[42:43]
	v_cndmask_b32_e64 v83, v83, v173, s[40:41]
	v_cndmask_b32_e64 v82, v82, v173, s[38:39]
	v_cndmask_b32_e64 v81, v81, v173, s[36:37]
	v_cndmask_b32_e64 v79, v79, v173, s[34:35]
	v_cndmask_b32_e64 v78, v78, v173, s[30:31]
	v_cndmask_b32_e64 v77, v77, v173, s[28:29]
	v_cndmask_b32_e64 v76, v76, v173, s[26:27]
	v_cndmask_b32_e64 v75, v75, v173, s[24:25]
	v_cndmask_b32_e64 v74, v74, v173, s[22:23]
	v_cndmask_b32_e64 v73, v73, v173, s[20:21]
	v_cndmask_b32_e64 v72, v72, v173, s[18:19]
	v_cndmask_b32_e64 v71, v71, v173, s[16:17]
	v_cndmask_b32_e64 v70, v70, v173, s[14:15]
	v_cndmask_b32_e64 v69, v69, v173, s[12:13]
	v_cndmask_b32_e64 v68, v68, v173, s[10:11]
	v_cndmask_b32_e64 v67, v67, v173, s[8:9]
	v_cndmask_b32_e64 v66, v66, v173, s[6:7]
	v_cndmask_b32_e64 v65, v65, v173, s[4:5]
	v_cndmask_b32_e32 v64, v64, v173, vcc
	v_readlane_b32 s49, v254, 43
	v_readlane_b32 s50, v254, 44
	v_readlane_b32 s51, v254, 45
	v_readlane_b32 s54, v254, 48
	v_readlane_b32 s55, v254, 49

.Lattn_inactive:
	s_mov_b32 m0, s8
	s_nop 0
	global_load_lds_dwordx4 v[240:241], off
	s_add_i32 m0, s8, 0x2000
	s_nop 0
	global_load_lds_dwordx4 v[242:243], off
	s_add_i32 m0, s8, 0x4000
	s_nop 0
	global_load_lds_dwordx4 v[244:245], off
	s_add_i32 m0, s8, 0x6000
	s_nop 0
	global_load_lds_dwordx4 v[246:247], off
	s_add_i32 m0, s8, 0x8000
	s_nop 0
	global_load_lds_dwordx4 v[248:249], off
	s_branch .LBB0_728
